# cmp pass 2: the eight importance quad-reductions batched (DPP stages back to back, one exec toggle, one base address with ds_write offsets) instead of eight nop-padded serial segments
# speedup vs baseline: 1.0070x; 1.0070x over previous
; #define LAS __attribute__((address_space(3)))
; __device__ __forceinline__ unsigned lds_addr(const LAS void* p) { return (unsigned)(size_t)p; }
; __device__ __forceinline__ void imp_accum(const f32x4 (&s)[4], float& carry, LAS float* impt  , int jb, int c, int q4, int lane) {
;     float rot[4];
; #pragma unroll
;     for (int T_ = 0; T_ < 4; ++T_) rot[T_] = __shfl(s[T_][3], (lane + 48) & 63);
; #pragma unroll
;     for (int T_ = 0; T_ < 4; ++T_) { const float prev = (q4 == 0) ? (T_ == 0 ? carry : rot[T_ == 0 ? 0 : T_ - 1]) : rot[T_];
;         float v = (s[T_][0] + s[T_][1]) + (s[T_][2] + s[T_][3]) + prev;
;         v += __builtin_bit_cast(float, __builtin_amdgcn_mov_dpp(__builtin_bit_cast(int, v), 0xB1, 0xF, 0xF, true));
;         v += __builtin_bit_cast(float, __builtin_amdgcn_mov_dpp(__builtin_bit_cast(int, v), 0x4E, 0xF, 0xF, true));
;         if ((c & 3) == 0) impt[jb + 4 * T_ + q4] = v; }
;     carry = rot[3];
; }
; __device__ __forceinline__ void cmp_phase(Frame& F) {
;     ...
;                     for (int q = 0; q < 4; ++q) { s0[T_][q] = __builtin_amdgcn_exp2f(s0[T_][q]); s1[T_][q] = __builtin_amdgcn_exp2f(s1[T_][q]); }
;                 imp_accum(s0, carry0, impA, kt * 16, c, kq, lane); imp_accum(s1, carry1, impB, kt * 16, c, kq, lane);
;                 pv_tile<2>(g0, g1, s0, s1, lds_addr(sb + K8TB) + vlane);
.LBB0_1585:
	s_and_b64 vcc, exec, s[22:23]
	s_cbranch_vccz .LBB0_1570
	v_exp_f32_e32 v138, v109
	v_exp_f32_e32 v109, v110
	v_exp_f32_e32 v110, v111
	v_exp_f32_e32 v134, v108
	v_exp_f32_e32 v108, v107
	v_exp_f32_e32 v107, v103
	v_exp_f32_e32 v103, v99
	ds_bpermute_b32 v146, v183, v110
	ds_bpermute_b32 v145, v183, v108
	ds_bpermute_b32 v144, v183, v107
	ds_bpermute_b32 v99, v183, v103
	v_add_f32_e32 v147, v134, v138
	v_add_f32_e32 v148, v109, v110
	s_waitcnt lgkmcnt(0)
	v_cndmask_b32_e64 v196, v146, v193, s[2:3]
	v_add_f32_e32 v147, v147, v148
	v_add_f32_e32 v196, v147, v196
	s_add_i32 s22, s79, s48
	v_add_u32_e32 v111, s22, v117
	v_exp_f32_e32 v140, v104
	v_exp_f32_e32 v105, v105
	v_exp_f32_e32 v104, v106
	v_cndmask_b32_e64 v197, v145, v146, s[2:3]
	v_add_f32_e32 v146, v140, v105
	v_add_f32_e32 v147, v104, v108
	v_add_f32_e32 v146, v146, v147
	v_add_f32_e32 v197, v146, v197
	v_exp_f32_e32 v106, v100
	v_exp_f32_e32 v101, v101
	v_exp_f32_e32 v100, v102
	v_cndmask_b32_e64 v198, v144, v145, s[2:3]
	v_add_f32_e32 v145, v106, v101
	v_add_f32_e32 v146, v100, v107
	v_add_f32_e32 v145, v145, v146
	v_add_f32_e32 v198, v145, v198
	v_exp_f32_e32 v102, v96
	v_exp_f32_e32 v97, v97
	v_exp_f32_e32 v96, v98
	v_cndmask_b32_e64 v199, v99, v144, s[2:3]
	v_add_f32_e32 v144, v102, v97
	v_add_f32_e32 v145, v96, v103
	v_add_f32_e32 v144, v144, v145
	v_add_f32_e32 v199, v144, v199
	v_exp_f32_e32 v91, v91
	v_exp_f32_e32 v98, v88
	v_exp_f32_e32 v144, v89
	v_exp_f32_e32 v89, v87
	v_exp_f32_e32 v88, v83
	v_exp_f32_e32 v87, v95
	ds_bpermute_b32 v147, v183, v91
	v_exp_f32_e32 v90, v90
	ds_bpermute_b32 v146, v183, v89
	ds_bpermute_b32 v145, v183, v88
	ds_bpermute_b32 v83, v183, v87
	v_add_f32_e32 v148, v98, v144
	v_add_f32_e32 v149, v90, v91
	s_waitcnt lgkmcnt(0)
	v_cndmask_b32_e64 v200, v147, v192, s[2:3]
	v_add_f32_e32 v148, v148, v149
	v_add_f32_e32 v200, v148, v200
	v_exp_f32_e32 v95, v84
	v_exp_f32_e32 v85, v85
	v_exp_f32_e32 v84, v86
	v_cndmask_b32_e64 v201, v146, v147, s[2:3]
	v_add_f32_e32 v147, v95, v85
	v_add_f32_e32 v148, v84, v89
	v_add_f32_e32 v147, v147, v148
	v_add_f32_e32 v201, v147, v201
	v_exp_f32_e32 v86, v80
	v_exp_f32_e32 v81, v81
	v_exp_f32_e32 v80, v82
	v_cndmask_b32_e64 v202, v145, v146, s[2:3]
	v_add_f32_e32 v146, v86, v81
	v_add_f32_e32 v147, v80, v88
	v_add_f32_e32 v146, v146, v147
	v_add_f32_e32 v202, v146, v202
	v_exp_f32_e32 v92, v92
	v_exp_f32_e32 v93, v93
	v_exp_f32_e32 v82, v94
	v_cndmask_b32_e64 v203, v83, v145, s[2:3]
	v_add_f32_e32 v145, v92, v93
	v_add_f32_e32 v146, v82, v87
	v_add_f32_e32 v145, v145, v146
	v_add_f32_e32 v203, v145, v203
	v_add_f32_dpp v196, v196, v196 quad_perm:[1,0,3,2] row_mask:0xf bank_mask:0xf bound_ctrl:1
	v_add_f32_dpp v197, v197, v197 quad_perm:[1,0,3,2] row_mask:0xf bank_mask:0xf bound_ctrl:1
	v_add_f32_dpp v198, v198, v198 quad_perm:[1,0,3,2] row_mask:0xf bank_mask:0xf bound_ctrl:1
	v_add_f32_dpp v199, v199, v199 quad_perm:[1,0,3,2] row_mask:0xf bank_mask:0xf bound_ctrl:1
	v_add_f32_dpp v200, v200, v200 quad_perm:[1,0,3,2] row_mask:0xf bank_mask:0xf bound_ctrl:1
	v_add_f32_dpp v201, v201, v201 quad_perm:[1,0,3,2] row_mask:0xf bank_mask:0xf bound_ctrl:1
	v_add_f32_dpp v202, v202, v202 quad_perm:[1,0,3,2] row_mask:0xf bank_mask:0xf bound_ctrl:1
	v_add_f32_dpp v203, v203, v203 quad_perm:[1,0,3,2] row_mask:0xf bank_mask:0xf bound_ctrl:1
	v_mov_b32_dpp v204, v196 quad_perm:[2,3,0,1] row_mask:0xf bank_mask:0xf bound_ctrl:1
	v_mov_b32_dpp v205, v197 quad_perm:[2,3,0,1] row_mask:0xf bank_mask:0xf bound_ctrl:1
	v_mov_b32_dpp v206, v198 quad_perm:[2,3,0,1] row_mask:0xf bank_mask:0xf bound_ctrl:1
	v_mov_b32_dpp v207, v199 quad_perm:[2,3,0,1] row_mask:0xf bank_mask:0xf bound_ctrl:1
	v_mov_b32_dpp v208, v200 quad_perm:[2,3,0,1] row_mask:0xf bank_mask:0xf bound_ctrl:1
	v_mov_b32_dpp v209, v201 quad_perm:[2,3,0,1] row_mask:0xf bank_mask:0xf bound_ctrl:1
	v_mov_b32_dpp v210, v202 quad_perm:[2,3,0,1] row_mask:0xf bank_mask:0xf bound_ctrl:1
	v_mov_b32_dpp v211, v203 quad_perm:[2,3,0,1] row_mask:0xf bank_mask:0xf bound_ctrl:1
	s_and_saveexec_b64 s[22:23], s[4:5]
	v_add_u32_e32 v212, 0x117c1, v111
	v_add_f32_e32 v196, v196, v204
	v_add_f32_e32 v197, v197, v205
	v_add_f32_e32 v198, v198, v206
	v_add_f32_e32 v199, v199, v207
	v_add_f32_e32 v200, v200, v208
	v_add_f32_e32 v201, v201, v209
	v_add_f32_e32 v202, v202, v210
	v_add_f32_e32 v203, v203, v211
	ds_write_b32 v212, v196
	ds_write_b32 v212, v197 offset:16
	ds_write_b32 v212, v198 offset:32
	ds_write_b32 v212, v199 offset:48
	ds_write_b32 v212, v200 offset:4096
	ds_write_b32 v212, v201 offset:4112
	ds_write_b32 v212, v202 offset:4128
	ds_write_b32 v212, v203 offset:4144
	s_or_b64 exec, exec, s[22:23]
	s_addk_i32 s37, 0x2400
	v_add_u32_e32 v145, s37, v173
	v_cvt_pk_bf16_f32 v146, v134, v138
	v_cvt_pk_bf16_f32 v147, v109, v110
	v_cvt_pk_bf16_f32 v148, v140, v105
	v_cvt_pk_bf16_f32 v149, v104, v108
	v_cvt_pk_bf16_f32 v104, v106, v101
	v_cvt_pk_bf16_f32 v105, v100, v107
	v_cvt_pk_bf16_f32 v106, v102, v97
	v_cvt_pk_bf16_f32 v107, v96, v103
	v_cvt_pk_bf16_f32 v100, v98, v144
	v_cvt_pk_bf16_f32 v101, v90, v91
	v_cvt_pk_bf16_f32 v102, v95, v85
	v_cvt_pk_bf16_f32 v103, v84, v89
	v_cvt_pk_bf16_f32 v84, v86, v81
	v_cvt_pk_bf16_f32 v85, v80, v88
	v_cvt_pk_bf16_f32 v86, v92, v93
	v_cvt_pk_bf16_f32 v87, v82, v87
	ds_read_b64_tr_b16 v[88:89], v145 offset:0
	ds_read_b64_tr_b16 v[90:91], v145 offset:0x1200
	ds_read_b64_tr_b16 v[92:93], v145 offset:0x2400
	ds_read_b64_tr_b16 v[94:95], v145 offset:0x3600
	ds_read_b64_tr_b16 v[108:109], v145 offset:32
	ds_read_b64_tr_b16 v[110:111], v145 offset:0x1220
	ds_read_b64_tr_b16 v[150:151], v145 offset:0x2420
	ds_read_b64_tr_b16 v[152:153], v145 offset:0x3620
	ds_read_b64_tr_b16 v[154:155], v145 offset:64
	ds_read_b64_tr_b16 v[156:157], v145 offset:0x1240
	ds_read_b64_tr_b16 v[158:159], v145 offset:0x2440
	ds_read_b64_tr_b16 v[160:161], v145 offset:0x3640
	s_setprio 1
	s_waitcnt lgkmcnt(8)
; #define SBAR() __builtin_amdgcn_sched_barrier(0)
; __device__ __forceinline__ bf16x8 ppack(const f32x4 a, const f32x4 b) { const u32x4 w = pack8f(a, b); return __builtin_bit_cast(bf16x8, w); }
; #define PV_RD(dt) do { TRRD(r[dt][0], vb, (dt) * 32); TRRD(r[dt][1], vb, (dt) * 32 + 4608); TRRD(r[dt][2], vb, (dt) * 32 + 9216); TRRD(r[dt][3], vb, (dt) * 32 + 9216 + 4608); } while (0)
; #define PV_W(n) asm volatile("s_waitcnt lgkmcnt(" #n ")" ::: "memory"); SBAR()
; template <int NG, class G> __device__ __forceinline__ void pv_tile(G& g0, G& g1, const f32x4 (&s0)[4], const f32x4 (&s1)[4], unsigned vb) {
;     const bf16x8 pa0 = ppack(s0[0], s0[1]), pa1 = ppack(s0[2], s0[3]);
;     bf16x8 pb0 = pa0, pb1 = pa1; if (NG == 2) { pb0 = ppack(s1[0], s1[1]); pb1 = ppack(s1[2], s1[3]); }
;     s16x4 r[8][4];
;     ...
;     PV_RD(0); PV_RD(1); PV_RD(2);
;     __builtin_amdgcn_s_setprio(1);
;     PV_W(8); PV_MM(0); SBAR(); PV_RD(3);
;     PV_W(8); PV_MM(1); SBAR(); PV_RD(4);
;     PV_W(8); PV_MM(2); SBAR(); PV_RD(5);
;     PV_W(8); PV_MM(3); SBAR(); PV_RD(6);
;     PV_W(8); PV_MM(4); SBAR(); PV_RD(7);
;     PV_W(8); PV_MM(5); PV_W(4); PV_MM(6); PV_W(0); PV_MM(7);
;     __builtin_amdgcn_s_setprio(0);
;     ...
; }
	v_mfma_f32_16x16x32_bf16 v[76:79], v[88:91], v[146:149], v[76:79]
	v_mfma_f32_16x16x32_bf16 v[44:47], v[88:91], v[100:103], v[44:47]
	v_mfma_f32_16x16x32_bf16 v[76:79], v[92:95], v[104:107], v[76:79]
	v_mfma_f32_16x16x32_bf16 v[44:47], v[92:95], v[84:87], v[44:47]
	ds_read_b64_tr_b16 v[88:89], v145 offset:0x60
	ds_read_b64_tr_b16 v[90:91], v145 offset:0x1260
	ds_read_b64_tr_b16 v[92:93], v145 offset:0x2460
	ds_read_b64_tr_b16 v[94:95], v145 offset:0x3660
	s_waitcnt lgkmcnt(8)
	v_mfma_f32_16x16x32_bf16 v[72:75], v[108:111], v[146:149], v[72:75]
	v_mfma_f32_16x16x32_bf16 v[40:43], v[108:111], v[100:103], v[40:43]
	v_mfma_f32_16x16x32_bf16 v[72:75], v[150:153], v[104:107], v[72:75]
	v_mfma_f32_16x16x32_bf16 v[40:43], v[150:153], v[84:87], v[40:43]
	ds_read_b64_tr_b16 v[108:109], v145 offset:0x80
	ds_read_b64_tr_b16 v[110:111], v145 offset:0x1280
	ds_read_b64_tr_b16 v[150:151], v145 offset:0x2480
	ds_read_b64_tr_b16 v[152:153], v145 offset:0x3680
	s_waitcnt lgkmcnt(8)
	v_mfma_f32_16x16x32_bf16 v[68:71], v[154:157], v[146:149], v[68:71]
	v_mfma_f32_16x16x32_bf16 v[36:39], v[154:157], v[100:103], v[36:39]
	v_mfma_f32_16x16x32_bf16 v[68:71], v[158:161], v[104:107], v[68:71]
	v_mfma_f32_16x16x32_bf16 v[36:39], v[158:161], v[84:87], v[36:39]
	ds_read_b64_tr_b16 v[154:155], v145 offset:0xa0
	ds_read_b64_tr_b16 v[156:157], v145 offset:0x12a0
	ds_read_b64_tr_b16 v[158:159], v145 offset:0x24a0
	ds_read_b64_tr_b16 v[160:161], v145 offset:0x36a0
	s_waitcnt lgkmcnt(8)
	v_mfma_f32_16x16x32_bf16 v[64:67], v[88:91], v[146:149], v[64:67]
	v_mfma_f32_16x16x32_bf16 v[32:35], v[88:91], v[100:103], v[32:35]
	v_mfma_f32_16x16x32_bf16 v[64:67], v[92:95], v[104:107], v[64:67]
	v_mfma_f32_16x16x32_bf16 v[32:35], v[92:95], v[84:87], v[32:35]
	ds_read_b64_tr_b16 v[88:89], v145 offset:0xc0
	ds_read_b64_tr_b16 v[90:91], v145 offset:0x12c0
	ds_read_b64_tr_b16 v[92:93], v145 offset:0x24c0
	ds_read_b64_tr_b16 v[94:95], v145 offset:0x36c0
	s_waitcnt lgkmcnt(8)
	v_mfma_f32_16x16x32_bf16 v[60:63], v[108:111], v[146:149], v[60:63]
	v_mfma_f32_16x16x32_bf16 v[28:31], v[108:111], v[100:103], v[28:31]
	v_mfma_f32_16x16x32_bf16 v[60:63], v[150:153], v[104:107], v[60:63]
	v_mfma_f32_16x16x32_bf16 v[28:31], v[150:153], v[84:87], v[28:31]
	ds_read_b64_tr_b16 v[108:109], v145 offset:0xe0
	ds_read_b64_tr_b16 v[110:111], v145 offset:0x12e0
	ds_read_b64_tr_b16 v[150:151], v145 offset:0x24e0
	ds_read_b64_tr_b16 v[152:153], v145 offset:0x36e0
	s_waitcnt lgkmcnt(8)
	v_mfma_f32_16x16x32_bf16 v[56:59], v[154:157], v[146:149], v[56:59]
	s_waitcnt lgkmcnt(4)
	v_mfma_f32_16x16x32_bf16 v[24:27], v[154:157], v[100:103], v[24:27]
	v_mfma_f32_16x16x32_bf16 v[56:59], v[158:161], v[104:107], v[56:59]
	v_mfma_f32_16x16x32_bf16 v[24:27], v[158:161], v[84:87], v[24:27]
	v_mfma_f32_16x16x32_bf16 v[52:55], v[88:91], v[146:149], v[52:55]
	s_waitcnt lgkmcnt(0)
	v_mfma_f32_16x16x32_bf16 v[20:23], v[88:91], v[100:103], v[20:23]
	v_mfma_f32_16x16x32_bf16 v[52:55], v[92:95], v[104:107], v[52:55]
	v_mfma_f32_16x16x32_bf16 v[20:23], v[92:95], v[84:87], v[20:23]
	v_mfma_f32_16x16x32_bf16 v[48:51], v[108:111], v[146:149], v[48:51]
	v_mfma_f32_16x16x32_bf16 v[16:19], v[108:111], v[100:103], v[16:19]
	v_mfma_f32_16x16x32_bf16 v[48:51], v[150:153], v[104:107], v[48:51]
	v_mfma_f32_16x16x32_bf16 v[16:19], v[150:153], v[84:87], v[16:19]
	s_setprio 0
	v_mov_b32_e32 v192, v83
	v_mov_b32_e32 v193, v99
	s_sub_i32 s59, s59, 64
	s_add_i32 s79, s79, 64
	s_and_b64 vcc, exec, s[54:55]
	s_cbranch_vccz .LBB0_1571
